# speedup vs baseline: 1.0208x; 1.0111x over previous
.LBB1_8:
	s_or_b64 exec, exec, s[4:5]
	s_waitcnt vmcnt(1)
	v_mov_b32_e32 v184, 1
	v_lshl_add_u32 v180, v176, 2, v172
	v_lshl_add_u32 v181, v177, 2, v172
	v_lshl_add_u32 v182, v178, 2, v172
	v_lshl_add_u32 v183, v179, 2, v172
	s_waitcnt lgkmcnt(0)
	ds_add_u32 v180, v184
	ds_add_u32 v181, v184
	ds_add_u32 v182, v184
	ds_add_u32 v183, v184
	s_waitcnt lgkmcnt(0)
	ds_read_b32 v151, v173
	s_waitcnt lgkmcnt(0)
	v_cvt_f32_i32_e32 v185, v151
	ds_write_b32 v173, v185 offset:256
	v_add_u32_e32 v10, v172, v2
	s_waitcnt vmcnt(1) lgkmcnt(0)
	s_barrier
	s_nop 0
	s_nop 0
	ds_read_b128 v[18:21], v10 offset:256
	ds_read_b128 v[22:25], v10 offset:288
	ds_read_b128 v[82:85], v10 offset:320
	ds_read_b128 v[86:89], v10 offset:352
	ds_read_b128 v[74:77], v10 offset:384
	ds_read_b128 v[78:81], v10 offset:416
	ds_read_b128 v[2:5], v213 offset:32768
	ds_read_b128 v[6:9], v213 offset:0
	ds_read_b128 v[66:69], v10 offset:448
	ds_read_b128 v[70:73], v10 offset:480
	ds_read_b128 v[10:13], v213 offset:1024
	s_waitcnt lgkmcnt(3)
	v_pk_mul_f32 v[26:27], v[8:9], v[20:21]
	v_pk_mul_f32 v[28:29], v[6:7], v[18:19]
	ds_read_b128 v[14:17], v213 offset:8192
	s_waitcnt lgkmcnt(1)
	v_pk_mul_f32 v[12:13], v[12:13], v[24:25]
	v_pk_mul_f32 v[10:11], v[10:11], v[22:23]
	v_pk_fma_f32 v[30:31], v[8:9], v[20:21], v[12:13]
	v_pk_fma_f32 v[32:33], v[6:7], v[18:19], v[10:11]
	v_cvt_pk_bf16_f32 v9, v12, v13
	v_cvt_pk_bf16_f32 v7, v26, v27
	v_cvt_pk_bf16_f32 v8, v10, v11
	v_cvt_pk_bf16_f32 v6, v28, v29
	ds_read_b128 v[10:13], v213 offset:33792
	s_nop 0
	v_mfma_f32_32x32x16_bf16 v[34:49], v[2:5], v[6:9], 0
	ds_read_b128 v[6:9], v213 offset:9216
	s_waitcnt lgkmcnt(2)
	v_mul_f32_e32 v26, v16, v20
	v_mul_f32_e32 v27, v17, v21
	v_pk_mul_f32 v[50:51], v[14:15], v[18:19]
	s_mov_b32 s4, 0x3727c5ac
	s_waitcnt lgkmcnt(0)
	v_pk_mul_f32 v[8:9], v[8:9], v[24:25]
	v_pk_mul_f32 v[28:29], v[6:7], v[22:23]
	v_pk_fma_f32 v[90:91], v[16:17], v[20:21], v[8:9]
	v_pk_fma_f32 v[92:93], v[14:15], v[18:19], v[28:29]
	ds_read_b128 v[14:17], v213 offset:2048
	v_cvt_pk_bf16_f32 v9, v8, v9
	v_cvt_pk_bf16_f32 v7, v26, v27
	v_cvt_pk_bf16_f32 v8, v28, v29
	ds_read_b128 v[26:29], v213 offset:3072
	v_cvt_pk_bf16_f32 v6, v50, v51
	s_waitcnt lgkmcnt(1)
	v_pk_mul_f32 v[94:95], v[14:15], v[82:83]
	s_mov_b32 s0, 0x3c800000
	v_mfma_f32_32x32x16_bf16 v[50:65], v[2:5], v[6:9], 0
	v_mul_f32_e32 v2, v16, v84
	v_mul_f32_e32 v3, v17, v85
	s_waitcnt lgkmcnt(0)
	v_mul_f32_e32 v4, v28, v88
	v_mul_f32_e32 v5, v29, v89
	v_pk_mul_f32 v[6:7], v[26:27], v[86:87]
	v_pk_fma_f32 v[8:9], v[16:17], v[84:85], v[4:5]
	v_cvt_pk_bf16_f32 v3, v2, v3
	v_pk_fma_f32 v[14:15], v[14:15], v[82:83], v[6:7]
	v_pk_add_f32 v[26:27], v[8:9], v[30:31]
	v_cvt_pk_bf16_f32 v5, v4, v5
	v_cvt_pk_bf16_f32 v4, v6, v7
	ds_read_b128 v[6:9], v213 offset:10240
	v_pk_add_f32 v[28:29], v[14:15], v[32:33]
	ds_read_b128 v[14:17], v213 offset:11264
	v_cvt_pk_bf16_f32 v2, v94, v95
	s_waitcnt lgkmcnt(1)
	v_pk_mul_f32 v[30:31], v[6:7], v[82:83]
	v_mov_b64_e32 v[152:153], s[4:5]
	v_mfma_f32_32x32x16_bf16 v[34:49], v[10:13], v[2:5], v[34:49]
	v_mul_f32_e32 v2, v8, v84
	v_mul_f32_e32 v3, v9, v85
	s_waitcnt lgkmcnt(0)
	v_mul_f32_e32 v4, v16, v88
	v_mul_f32_e32 v5, v17, v89
	v_pk_mul_f32 v[14:15], v[14:15], v[86:87]
	v_pk_fma_f32 v[8:9], v[8:9], v[84:85], v[4:5]
	v_pk_fma_f32 v[6:7], v[6:7], v[82:83], v[14:15]
	v_cvt_pk_bf16_f32 v5, v4, v5
	v_cvt_pk_bf16_f32 v3, v2, v3
	v_cvt_pk_bf16_f32 v4, v14, v15
	v_pk_add_f32 v[32:33], v[8:9], v[90:91]
	v_pk_add_f32 v[90:91], v[6:7], v[92:93]
	ds_read_b128 v[6:9], v213 offset:34816
	ds_read_b128 v[14:17], v213 offset:4096
	v_cvt_pk_bf16_f32 v2, v30, v31
	s_mov_b32 s13, 0
	s_mov_b64 s[6:7], 0
	v_mfma_f32_32x32x16_bf16 v[50:65], v[10:13], v[2:5], v[50:65]
	ds_read_b128 v[2:5], v213 offset:5120
	ds_read_b128 v[10:13], v213 offset:12288
	s_waitcnt lgkmcnt(2)
	v_pk_mul_f32 v[30:31], v[16:17], v[76:77]
	v_pk_mul_f32 v[92:93], v[14:15], v[74:75]
	s_waitcnt lgkmcnt(1)
	v_pk_mul_f32 v[4:5], v[4:5], v[80:81]
	v_pk_mul_f32 v[94:95], v[2:3], v[78:79]
	v_pk_fma_f32 v[2:3], v[16:17], v[76:77], v[4:5]
	v_cvt_pk_bf16_f32 v5, v4, v5
	v_pk_add_f32 v[96:97], v[2:3], v[26:27]
	v_cvt_pk_bf16_f32 v3, v30, v31
	v_cvt_pk_bf16_f32 v4, v94, v95
	v_cvt_pk_bf16_f32 v2, v92, v93
	v_pk_fma_f32 v[14:15], v[14:15], v[74:75], v[94:95]
	s_waitcnt lgkmcnt(0)
	v_pk_mul_f32 v[30:31], v[10:11], v[74:75]
	v_mfma_f32_32x32x16_bf16 v[34:49], v[6:9], v[2:5], v[34:49]
	ds_read_b128 v[2:5], v213 offset:13312
	v_add_f32_e32 v98, v14, v28
	v_add_f32_e32 v99, v15, v29
	ds_read_b128 v[14:17], v213 offset:35840
	v_pk_mul_f32 v[26:27], v[12:13], v[76:77]
	s_waitcnt lgkmcnt(1)
	v_pk_mul_f32 v[4:5], v[4:5], v[80:81]
	v_pk_mul_f32 v[28:29], v[2:3], v[78:79]
	v_pk_fma_f32 v[2:3], v[12:13], v[76:77], v[4:5]
	v_pk_fma_f32 v[10:11], v[10:11], v[74:75], v[28:29]
	v_pk_add_f32 v[32:33], v[2:3], v[32:33]
	v_pk_add_f32 v[92:93], v[10:11], v[90:91]
	ds_read_b128 v[10:13], v213 offset:6144
	v_cvt_pk_bf16_f32 v5, v4, v5
	v_cvt_pk_bf16_f32 v3, v26, v27
	v_cvt_pk_bf16_f32 v4, v28, v29
	ds_read_b128 v[26:29], v213 offset:7168
	v_cvt_pk_bf16_f32 v2, v30, v31
	s_waitcnt lgkmcnt(1)
	v_pk_mul_f32 v[30:31], v[10:11], v[66:67]
	v_mfma_f32_32x32x16_bf16 v[50:65], v[6:9], v[2:5], v[50:65]
	v_mul_f32_e32 v2, v12, v68
	v_mul_f32_e32 v3, v13, v69
	s_waitcnt lgkmcnt(0)
	v_mul_f32_e32 v4, v28, v72
	v_mul_f32_e32 v5, v29, v73
	v_pk_mul_f32 v[6:7], v[26:27], v[70:71]
	v_pk_fma_f32 v[8:9], v[12:13], v[68:69], v[4:5]
	v_cvt_pk_bf16_f32 v3, v2, v3
	v_pk_fma_f32 v[10:11], v[10:11], v[66:67], v[6:7]
	v_pk_add_f32 v[94:95], v[8:9], v[96:97]
	v_cvt_pk_bf16_f32 v5, v4, v5
	v_cvt_pk_bf16_f32 v4, v6, v7
	ds_read_b128 v[6:9], v213 offset:14336
	v_pk_add_f32 v[96:97], v[10:11], v[98:99]
	ds_read_b128 v[10:13], v213 offset:15360
	v_cvt_pk_bf16_f32 v2, v30, v31
	s_waitcnt lgkmcnt(1)
	v_pk_mul_f32 v[30:31], v[6:7], v[66:67]
	v_mfma_f32_32x32x16_bf16 v[34:49], v[14:17], v[2:5], v[34:49]
	s_waitcnt lgkmcnt(0)
	v_mul_f32_e32 v10, v10, v70
	v_mul_f32_e32 v11, v11, v71
	v_mul_f32_e32 v2, v8, v68
	v_mul_f32_e32 v3, v9, v69
	v_pk_mul_f32 v[4:5], v[12:13], v[72:73]
	v_pk_fma_f32 v[6:7], v[6:7], v[66:67], v[10:11]
	v_pk_fma_f32 v[8:9], v[8:9], v[68:69], v[4:5]
	v_pk_add_f32 v[92:93], v[6:7], v[92:93]
	v_cvt_pk_bf16_f32 v3, v2, v3
	v_pk_add_f32 v[90:91], v[8:9], v[32:33]
	v_cvt_pk_bf16_f32 v5, v4, v5
	v_cvt_pk_bf16_f32 v4, v10, v11
	ds_read_b128 v[26:29], v213 offset:36864
	ds_read_b128 v[6:9], v213 offset:16384
	v_cvt_pk_bf16_f32 v2, v30, v31
	ds_read_b128 v[98:101], v213 offset:25600
	ds_read_b128 v[102:105], v213 offset:37888
	v_mfma_f32_32x32x16_bf16 v[50:65], v[14:17], v[2:5], v[50:65]
	ds_read_b128 v[2:5], v213 offset:17408
	ds_read_b128 v[30:33], v213 offset:24576
	s_waitcnt lgkmcnt(4)
	v_pk_mul_f32 v[12:13], v[6:7], v[18:19]
	v_pk_mul_f32 v[10:11], v[8:9], v[20:21]
	s_waitcnt lgkmcnt(1)
	v_pk_mul_f32 v[14:15], v[2:3], v[22:23]
	v_pk_mul_f32 v[22:23], v[98:99], v[22:23]
	v_pk_fma_f32 v[112:113], v[6:7], v[18:19], v[14:15]
	s_waitcnt lgkmcnt(0)
	v_pk_mul_f32 v[114:115], v[30:31], v[18:19]
	v_pk_fma_f32 v[118:119], v[30:31], v[18:19], v[22:23]
	v_pk_mul_f32 v[4:5], v[4:5], v[24:25]
	v_pk_mul_f32 v[106:107], v[32:33], v[20:21]
	v_pk_mul_f32 v[24:25], v[100:101], v[24:25]
	ds_read_b128 v[98:101], v213 offset:18432
	v_cvt_pk_bf16_f32 v19, v106, v107
	ds_read_b128 v[106:109], v213 offset:19456
	v_pk_fma_f32 v[110:111], v[8:9], v[20:21], v[4:5]
	v_cvt_pk_bf16_f32 v5, v4, v5
	v_cvt_pk_bf16_f32 v3, v10, v11
	v_cvt_pk_bf16_f32 v4, v14, v15
	s_waitcnt lgkmcnt(0)
	v_pk_mul_f32 v[106:107], v[106:107], v[86:87]
	v_cvt_pk_bf16_f32 v2, v12, v13
	v_pk_mul_f32 v[120:121], v[98:99], v[82:83]
	v_pk_mul_f32 v[108:109], v[108:109], v[88:89]
	v_pk_fma_f32 v[98:99], v[98:99], v[82:83], v[106:107]
	v_mfma_f32_32x32x16_bf16 v[2:17], v[26:29], v[2:5], 0
	v_cvt_pk_bf16_f32 v18, v114, v115
	v_mul_f32_e32 v114, v100, v84
	v_mul_f32_e32 v115, v101, v85
	v_fma_f32 v100, v100, v84, v108
	v_fma_f32 v101, v101, v85, v109
	v_pk_add_f32 v[124:125], v[98:99], v[112:113]
	v_pk_add_f32 v[122:123], v[100:101], v[110:111]
	v_cvt_pk_bf16_f32 v101, v108, v109
	v_cvt_pk_bf16_f32 v100, v106, v107
	ds_read_b128 v[106:109], v213 offset:26624
	v_pk_fma_f32 v[116:117], v[32:33], v[20:21], v[24:25]
	v_cvt_pk_bf16_f32 v21, v24, v25
	v_cvt_pk_bf16_f32 v20, v22, v23
	ds_read_b128 v[110:113], v213 offset:27648
	v_cvt_pk_bf16_f32 v99, v114, v115
	v_mfma_f32_32x32x16_bf16 v[18:33], v[26:29], v[18:21], 0
	v_cvt_pk_bf16_f32 v98, v120, v121
	s_waitcnt lgkmcnt(1)
	v_mul_f32_e32 v114, v106, v82
	v_mul_f32_e32 v115, v107, v83
	s_waitcnt lgkmcnt(0)
	v_pk_mul_f32 v[86:87], v[110:111], v[86:87]
	v_pk_mul_f32 v[88:89], v[112:113], v[88:89]
	v_pk_fma_f32 v[82:83], v[106:107], v[82:83], v[86:87]
	v_mfma_f32_32x32x16_bf16 v[2:17], v[102:105], v[98:101], v[2:17]
	v_mul_f32_e32 v98, v108, v84
	v_mul_f32_e32 v99, v109, v85
	v_fma_f32 v84, v108, v84, v88
	v_fma_f32 v85, v109, v85, v89
	v_add_f32_e32 v108, v82, v118
	v_add_f32_e32 v109, v83, v119
	v_cvt_pk_bf16_f32 v83, v98, v99
	v_pk_add_f32 v[106:107], v[84:85], v[116:117]
	v_cvt_pk_bf16_f32 v85, v88, v89
	v_cvt_pk_bf16_f32 v84, v86, v87
	ds_read_b128 v[86:89], v213 offset:38912
	ds_read_b128 v[98:101], v213 offset:20480
	v_cvt_pk_bf16_f32 v82, v114, v115
	s_waitcnt lgkmcnt(0)
	v_pk_mul_f32 v[110:111], v[100:101], v[76:77]
	v_mfma_f32_32x32x16_bf16 v[18:33], v[102:105], v[82:85], v[18:33]
	ds_read_b128 v[82:85], v213 offset:21504
	ds_read_b128 v[102:105], v213 offset:28672
	v_mul_f32_e32 v112, v98, v74
	v_mul_f32_e32 v113, v99, v75
	s_waitcnt lgkmcnt(1)
	v_pk_mul_f32 v[84:85], v[84:85], v[80:81]
	v_pk_mul_f32 v[114:115], v[82:83], v[78:79]
	v_pk_fma_f32 v[82:83], v[100:101], v[76:77], v[84:85]
	v_cvt_pk_bf16_f32 v85, v84, v85
	v_pk_add_f32 v[116:117], v[82:83], v[122:123]
	v_cvt_pk_bf16_f32 v83, v110, v111
	v_cvt_pk_bf16_f32 v84, v114, v115
	v_cvt_pk_bf16_f32 v82, v112, v113
	v_pk_fma_f32 v[98:99], v[98:99], v[74:75], v[114:115]
	s_waitcnt lgkmcnt(0)
	v_pk_mul_f32 v[112:113], v[102:103], v[74:75]
	v_mfma_f32_32x32x16_bf16 v[2:17], v[86:89], v[82:85], v[2:17]
	ds_read_b128 v[82:85], v213 offset:29696
	v_add_f32_e32 v118, v98, v124
	v_add_f32_e32 v119, v99, v125
	v_mul_f32_e32 v110, v104, v76
	v_mul_f32_e32 v111, v105, v77
	ds_read_b128 v[98:101], v213 offset:39936
	s_waitcnt lgkmcnt(1)
	v_pk_mul_f32 v[78:79], v[82:83], v[78:79]
	v_pk_mul_f32 v[80:81], v[84:85], v[80:81]
	v_pk_fma_f32 v[74:75], v[102:103], v[74:75], v[78:79]
	v_pk_fma_f32 v[76:77], v[104:105], v[76:77], v[80:81]
	v_pk_add_f32 v[104:105], v[74:75], v[108:109]
	v_pk_add_f32 v[102:103], v[76:77], v[106:107]
	v_cvt_pk_bf16_f32 v77, v80, v81
	v_cvt_pk_bf16_f32 v76, v78, v79
	ds_read_b128 v[78:81], v213 offset:22528
	ds_read_b128 v[82:85], v213 offset:23552
	v_cvt_pk_bf16_f32 v75, v110, v111
	v_cvt_pk_bf16_f32 v74, v112, v113
	s_waitcnt lgkmcnt(0)
	v_pk_mul_f32 v[82:83], v[82:83], v[70:71]
	v_mfma_f32_32x32x16_bf16 v[18:33], v[86:89], v[74:77], v[18:33]
	v_mul_f32_e32 v74, v80, v68
	v_mul_f32_e32 v75, v81, v69
	v_mul_f32_e32 v76, v84, v72
	v_mul_f32_e32 v77, v85, v73
	v_mul_f32_e32 v86, v78, v66
	v_mul_f32_e32 v87, v79, v67
	v_pk_fma_f32 v[80:81], v[80:81], v[68:69], v[76:77]
	v_pk_fma_f32 v[78:79], v[78:79], v[66:67], v[82:83]
	v_cvt_pk_bf16_f32 v75, v74, v75
	v_pk_add_f32 v[88:89], v[80:81], v[116:117]
	v_pk_add_f32 v[106:107], v[78:79], v[118:119]
	ds_read_b128 v[78:81], v213 offset:30720
	v_cvt_pk_bf16_f32 v77, v76, v77
	v_cvt_pk_bf16_f32 v76, v82, v83
	ds_read_b128 v[82:85], v213 offset:31744
	v_cvt_pk_bf16_f32 v74, v86, v87
	s_waitcnt lgkmcnt(0)
	v_pk_mul_f32 v[72:73], v[84:85], v[72:73]
	v_mfma_f32_32x32x16_bf16 v[2:17], v[98:101], v[74:77], v[2:17]
	v_mul_f32_e32 v74, v80, v68
	v_mul_f32_e32 v75, v81, v69
	v_fma_f32 v68, v80, v68, v72
	v_fma_f32 v69, v81, v69, v73
	v_mul_f32_e32 v70, v82, v70
	v_mul_f32_e32 v71, v83, v71
	v_pk_add_f32 v[84:85], v[68:69], v[102:103]
	v_cvt_pk_bf16_f32 v69, v72, v73
	v_add_f32_e32 v72, v97, v96
	v_add_f32_e32 v73, v94, v95
	v_pk_mul_f32 v[76:77], v[78:79], v[66:67]
	v_pk_fma_f32 v[66:67], v[78:79], v[66:67], v[70:71]
	v_add_f32_e32 v72, v72, v73
	v_pk_add_f32 v[86:87], v[66:67], v[104:105]
	v_mov_b32_e32 v66, v72
	s_nop 1
	v_permlane32_swap_b32_e32 v72, v66
	v_add_f32_e32 v66, v72, v66
	v_cvt_pk_bf16_f32 v67, v74, v75
	v_rcp_f32_e32 v74, v66
	v_cvt_pk_bf16_f32 v68, v70, v71
	v_cvt_pk_bf16_f32 v66, v76, v77
	v_pk_mul_f32 v[70:71], v[46:47], v[74:75] op_sel_hi:[1,0]
	s_nop 0
	v_mfma_f32_32x32x16_bf16 v[18:33], v[98:101], v[66:69], v[18:33]
	v_mul_f32_e32 v66, v42, v74
	v_mul_f32_e32 v67, v43, v74
	v_add_f32_e32 v42, v93, v92
	v_add_f32_e32 v43, v90, v91
	v_pk_mul_f32 v[68:69], v[44:45], v[74:75] op_sel_hi:[1,0]
	v_add_f32_e32 v42, v42, v43
	v_mov_b32_e32 v43, v42
	s_nop 1
	v_permlane32_swap_b32_e32 v42, v43
	v_add_f32_e32 v42, v42, v43
	v_rcp_f32_e32 v42, v42
	v_add_f32_e32 v44, v107, v106
	v_add_f32_e32 v45, v88, v89
	v_pk_mul_f32 v[72:73], v[48:49], v[74:75] op_sel_hi:[1,0]
	v_add_f32_e32 v44, v44, v45
	v_pk_mul_f32 v[36:37], v[36:37], v[74:75] op_sel_hi:[1,0]
	v_pk_mul_f32 v[38:39], v[38:39], v[74:75] op_sel_hi:[1,0]
	v_pk_mul_f32 v[40:41], v[40:41], v[74:75] op_sel_hi:[1,0]
	v_pk_mul_f32 v[34:35], v[34:35], v[74:75] op_sel_hi:[1,0]
	v_pk_mul_f32 v[74:75], v[58:59], v[42:43] op_sel_hi:[1,0]
	v_pk_mul_f32 v[78:79], v[60:61], v[42:43] op_sel_hi:[1,0]
	v_pk_mul_f32 v[80:81], v[62:63], v[42:43] op_sel_hi:[1,0]
	v_pk_mul_f32 v[82:83], v[64:65], v[42:43] op_sel_hi:[1,0]
	v_pk_mul_f32 v[92:93], v[52:53], v[42:43] op_sel_hi:[1,0]
	v_mov_b32_e32 v43, v44
	s_nop 1
	v_permlane32_swap_b32_e32 v44, v43
	v_add_f32_e32 v43, v44, v43
	v_rcp_f32_e32 v76, v43
	v_pk_mul_f32 v[96:97], v[54:55], v[42:43] op_sel_hi:[1,0]
	v_pk_mul_f32 v[94:95], v[56:57], v[42:43] op_sel_hi:[1,0]
	v_pk_mul_f32 v[98:99], v[50:51], v[42:43] op_sel_hi:[1,0]
	v_pk_mul_f32 v[100:101], v[4:5], v[76:77] op_sel_hi:[1,0]
	v_pk_mov_b32 v[4:5], v[86:87], v[84:85] op_sel:[1,0]
	v_mov_b32_e32 v87, v85
	v_pk_add_f32 v[4:5], v[4:5], v[86:87]
	v_pk_mul_f32 v[102:103], v[6:7], v[76:77] op_sel_hi:[1,0]
	v_pk_add_f32 v[104:105], v[4:5], v[4:5] op_sel:[0,1] op_sel_hi:[1,0]
	v_cvt_pk_bf16_f32 v7, v40, v41
	ds_read_b128 v[84:87], v150 offset:52224
	ds_read_b128 v[50:53], v150 offset:35840
	ds_read_b128 v[54:57], v150 offset:36864
	ds_read_b128 v[58:61], v150 offset:37888
	ds_read_b128 v[62:65], v150 offset:38912
	v_cvt_pk_bf16_f32 v6, v38, v39
	v_cvt_pk_bf16_f32 v5, v36, v37
	v_cvt_pk_bf16_f32 v4, v34, v35
	ds_read_b128 v[88:91], v150 offset:53248
	ds_read_b128 v[34:37], v150 offset:39936
	ds_read_b128 v[38:41], v150 offset:40960
	ds_read_b128 v[42:45], v150 offset:41984
	ds_read_b128 v[46:49], v150 offset:43008
	v_cvt_pk_bf16_f32 v95, v94, v95
	v_cvt_pk_bf16_f32 v94, v96, v97
	v_cvt_pk_bf16_f32 v93, v92, v93
	v_cvt_pk_bf16_f32 v92, v98, v99
	s_waitcnt lgkmcnt(5)
	v_mfma_f32_32x32x16_bf16 v[50:65], v[84:87], v[4:7], v[50:65]
	v_mul_f32_e32 v10, v10, v76
	v_mul_f32_e32 v11, v11, v76
	v_mul_f32_e32 v12, v12, v76
	v_mul_f32_e32 v13, v13, v76
	v_mul_f32_e32 v8, v8, v76
	v_mul_f32_e32 v9, v9, v76
	v_mov_b32_e32 v77, v104
	s_nop 1
	v_permlane32_swap_b32_e32 v104, v77
	v_cvt_pk_bf16_f32 v73, v72, v73
	s_waitcnt lgkmcnt(0)
	v_mfma_f32_32x32x16_bf16 v[34:49], v[84:87], v[92:95], v[34:49]
	v_cvt_pk_bf16_f32 v72, v70, v71
	v_cvt_pk_bf16_f32 v70, v66, v67
	v_add_f32_e32 v66, v104, v77
	v_cvt_pk_bf16_f32 v71, v68, v69
	v_rcp_f32_e32 v104, v66
	v_cvt_pk_bf16_f32 v69, v82, v83
	v_cvt_pk_bf16_f32 v68, v80, v81
	v_cvt_pk_bf16_f32 v67, v78, v79
	v_cvt_pk_bf16_f32 v66, v74, v75
	ds_read_b128 v[78:81], v150 offset:54272
	v_mfma_f32_32x32x16_bf16 v[50:65], v[88:91], v[70:73], v[50:65]
	v_mul_f32_e32 v2, v2, v76
	v_mul_f32_e32 v3, v3, v76
	v_mul_f32_e32 v20, v20, v104
	v_mul_f32_e32 v21, v21, v104
	v_cvt_pk_bf16_f32 v85, v8, v9
	v_cvt_pk_bf16_f32 v82, v2, v3
	v_pk_mul_f32 v[2:3], v[22:23], v[104:105] op_sel_hi:[1,0]
	v_pk_mul_f32 v[8:9], v[24:25], v[104:105] op_sel_hi:[1,0]
	v_pk_mul_f32 v[18:19], v[18:19], v[104:105] op_sel_hi:[1,0]
	v_mfma_f32_32x32x16_bf16 v[34:49], v[88:91], v[66:69], v[34:49]
	v_cvt_pk_bf16_f32 v84, v102, v103
	v_cvt_pk_bf16_f32 v83, v100, v101
	ds_read_b128 v[86:89], v150 offset:55296
	v_cvt_pk_bf16_f32 v99, v8, v9
	v_cvt_pk_bf16_f32 v98, v2, v3
	v_cvt_pk_bf16_f32 v97, v20, v21
	v_cvt_pk_bf16_f32 v96, v18, v19
	s_waitcnt lgkmcnt(1)
	v_mfma_f32_32x32x16_bf16 v[50:65], v[78:81], v[82:85], v[50:65]
	v_mul_f32_e32 v2, v14, v76
	v_mul_f32_e32 v3, v15, v76
	v_mul_f32_e32 v8, v16, v76
	v_mul_f32_e32 v9, v17, v76
	v_mul_f32_e32 v14, v26, v104
	v_mul_f32_e32 v15, v27, v104
	v_cvt_pk_bf16_f32 v77, v8, v9
	v_cvt_pk_bf16_f32 v76, v2, v3
	v_cvt_pk_bf16_f32 v74, v10, v11
	v_pk_mul_f32 v[2:3], v[28:29], v[104:105] op_sel_hi:[1,0]
	v_mfma_f32_32x32x16_bf16 v[34:49], v[78:81], v[96:99], v[34:49]
	v_mul_f32_e32 v8, v30, v104
	v_mul_f32_e32 v9, v31, v104
	v_mul_f32_e32 v10, v32, v104
	v_mul_f32_e32 v11, v33, v104
	v_cvt_pk_bf16_f32 v75, v12, v13
	v_cvt_pk_bf16_f32 v81, v10, v11
	v_cvt_pk_bf16_f32 v80, v8, v9
	v_cvt_pk_bf16_f32 v79, v2, v3
	v_cvt_pk_bf16_f32 v78, v14, v15
	s_waitcnt lgkmcnt(0)
	v_mfma_f32_32x32x16_bf16 v[50:65], v[86:89], v[74:77], v[50:65]
	v_mfma_f32_32x32x16_bf16 v[34:49], v[86:89], v[78:81], v[34:49]
	ds_read_b128 v[86:89], v150 offset:56320
	ds_read_b128 v[18:21], v150 offset:44032
	ds_read_b128 v[22:25], v150 offset:45056
	ds_read_b128 v[26:29], v150 offset:46080
	ds_read_b128 v[30:33], v150 offset:47104
	ds_read_b128 v[100:103], v150 offset:57344
	s_waitcnt lgkmcnt(1)
	v_mfma_f32_32x32x16_bf16 v[18:33], v[86:89], v[4:7], v[18:33]
	ds_read_b128 v[2:5], v150 offset:48128
	ds_read_b128 v[6:9], v150 offset:49152
	ds_read_b128 v[10:13], v150 offset:50176
	ds_read_b128 v[14:17], v150 offset:51200
	s_waitcnt lgkmcnt(0)
	v_mfma_f32_32x32x16_bf16 v[2:17], v[86:89], v[92:95], v[2:17]
	v_mfma_f32_32x32x16_bf16 v[18:33], v[100:103], v[70:73], v[18:33]
	v_mfma_f32_32x32x16_bf16 v[2:17], v[100:103], v[66:69], v[2:17]
	ds_read_b128 v[66:69], v150 offset:58368
	ds_read_b128 v[70:73], v150 offset:59392
	s_waitcnt lgkmcnt(1)
	v_mfma_f32_32x32x16_bf16 v[18:33], v[66:69], v[82:85], v[18:33]
	v_mfma_f32_32x32x16_bf16 v[2:17], v[66:69], v[96:99], v[2:17]
	s_waitcnt lgkmcnt(0)
	v_mfma_f32_32x32x16_bf16 v[18:33], v[70:73], v[74:77], v[18:33]
	v_mfma_f32_32x32x16_bf16 v[2:17], v[70:73], v[78:81], v[2:17]
	s_nop 10
	v_mul_f32_e32 v66, v22, v22
	v_mul_f32_e32 v67, v23, v23
	v_mul_f32_e32 v68, v30, v30
	v_mul_f32_e32 v69, v31, v31
	v_mul_f32_e32 v70, v24, v24
	v_mul_f32_e32 v71, v25, v25
	v_pk_mul_f32 v[72:73], v[32:33], v[32:33]
	v_pk_mul_f32 v[74:75], v[20:21], v[20:21]
	v_pk_mul_f32 v[76:77], v[28:29], v[28:29]
	v_pk_mul_f32 v[78:79], v[26:27], v[26:27]
	v_pk_mul_f32 v[80:81], v[18:19], v[18:19]
	v_pk_fma_f32 v[78:79], v[58:59], v[58:59], v[78:79]
	v_pk_fma_f32 v[76:77], v[60:61], v[60:61], v[76:77]
	v_pk_fma_f32 v[74:75], v[52:53], v[52:53], v[74:75]
	v_pk_fma_f32 v[72:73], v[64:65], v[64:65], v[72:73]
	v_pk_fma_f32 v[70:71], v[56:57], v[56:57], v[70:71]
	v_pk_fma_f32 v[68:69], v[62:63], v[62:63], v[68:69]
	v_pk_fma_f32 v[66:67], v[54:55], v[54:55], v[66:67]
	v_pk_fma_f32 v[80:81], v[50:51], v[50:51], v[80:81]
	v_pk_add_f32 v[66:67], v[66:67], v[68:69]
	v_pk_add_f32 v[68:69], v[70:71], v[72:73]
	v_pk_add_f32 v[70:71], v[74:75], v[76:77]
	v_pk_add_f32 v[72:73], v[80:81], v[78:79]
	v_pk_add_f32 v[68:69], v[70:71], v[68:69]
	v_pk_add_f32 v[66:67], v[72:73], v[66:67]
	v_pk_mul_f32 v[72:73], v[14:15], v[14:15]
	v_pk_mov_b32 v[70:71], v[66:67], v[68:69] op_sel:[1,0]
	v_mov_b32_e32 v67, v69
	v_pk_add_f32 v[66:67], v[70:71], v[66:67]
	v_pk_mul_f32 v[70:71], v[6:7], v[6:7]
	v_pk_mul_f32 v[74:75], v[8:9], v[8:9]
	v_pk_mul_f32 v[76:77], v[16:17], v[16:17]
	v_pk_mul_f32 v[78:79], v[4:5], v[4:5]
	v_pk_mul_f32 v[80:81], v[12:13], v[12:13]
	v_pk_mul_f32 v[82:83], v[10:11], v[10:11]
	v_pk_mul_f32 v[84:85], v[2:3], v[2:3]
	v_pk_fma_f32 v[82:83], v[42:43], v[42:43], v[82:83]
	v_pk_fma_f32 v[80:81], v[44:45], v[44:45], v[80:81]
	v_pk_fma_f32 v[78:79], v[36:37], v[36:37], v[78:79]
	v_pk_fma_f32 v[76:77], v[48:49], v[48:49], v[76:77]
	v_pk_fma_f32 v[74:75], v[40:41], v[40:41], v[74:75]
	v_pk_fma_f32 v[72:73], v[46:47], v[46:47], v[72:73]
	v_pk_fma_f32 v[70:71], v[38:39], v[38:39], v[70:71]
	v_pk_fma_f32 v[84:85], v[34:35], v[34:35], v[84:85]
	v_pk_add_f32 v[70:71], v[70:71], v[72:73]
	v_pk_add_f32 v[72:73], v[74:75], v[76:77]
	v_pk_add_f32 v[74:75], v[78:79], v[80:81]
	v_pk_add_f32 v[76:77], v[84:85], v[82:83]
	v_pk_add_f32 v[72:73], v[74:75], v[72:73]
	v_pk_add_f32 v[70:71], v[76:77], v[70:71]
	v_pk_add_f32 v[66:67], v[66:67], v[66:67] op_sel:[0,1] op_sel_hi:[1,0]
	v_add_f32_e32 v70, v71, v70
	v_add_f32_e32 v71, v72, v73
	v_mov_b32_e32 v69, v66
	v_add_f32_e32 v70, v70, v71
	s_nop 0
	v_permlane32_swap_b32_e32 v66, v69
	v_mov_b32_e32 v68, v70
	s_nop 1
	v_permlane32_swap_b32_e32 v70, v68
	v_mov_b32_e32 v71, v66
	v_pk_add_f32 v[66:67], v[70:71], v[68:69]
	v_pk_fma_f32 v[66:67], v[66:67], s[0:1], v[152:153] op_sel_hi:[1,0,0]
	s_mov_b32 s1, 0x800000
	v_rsq_f32_e32 v68, v67
	s_nop 0
	v_pk_mul_f32 v[158:159], v[50:51], v[68:69] op_sel_hi:[1,0]
	v_pk_mul_f32 v[50:51], v[18:19], v[68:69] op_sel_hi:[1,0]
	v_pk_mul_f32 v[80:81], v[60:61], v[68:69] op_sel_hi:[1,0]
	v_pk_mul_f32 v[60:61], v[28:29], v[68:69] op_sel_hi:[1,0]
	v_pk_mul_f32 v[78:79], v[58:59], v[68:69] op_sel_hi:[1,0]
	v_pk_mul_f32 v[160:161], v[52:53], v[68:69] op_sel_hi:[1,0]
	v_pk_mul_f32 v[82:83], v[54:55], v[68:69] op_sel_hi:[1,0]
	v_rsq_f32_e32 v28, v66
	v_pk_mul_f32 v[168:169], v[56:57], v[68:69] op_sel_hi:[1,0]
	v_pk_mul_f32 v[58:59], v[26:27], v[68:69] op_sel_hi:[1,0]
	v_pk_mul_f32 v[52:53], v[20:21], v[68:69] op_sel_hi:[1,0]
	v_pk_mul_f32 v[54:55], v[22:23], v[68:69] op_sel_hi:[1,0]
	v_pk_mul_f32 v[56:57], v[24:25], v[68:69] op_sel_hi:[1,0]
	v_pk_mul_f32 v[18:19], v[42:43], v[28:29] op_sel_hi:[1,0]
	v_pk_mul_f32 v[20:21], v[44:45], v[28:29] op_sel_hi:[1,0]
	v_pk_mul_f32 v[22:23], v[46:47], v[28:29] op_sel_hi:[1,0]
	v_pk_mul_f32 v[26:27], v[48:49], v[28:29] op_sel_hi:[1,0]
	v_pk_mul_f32 v[162:163], v[34:35], v[28:29] op_sel_hi:[1,0]
	v_pk_mul_f32 v[164:165], v[36:37], v[28:29] op_sel_hi:[1,0]
	v_pk_mul_f32 v[166:167], v[38:39], v[28:29] op_sel_hi:[1,0]
	v_pk_mul_f32 v[24:25], v[40:41], v[28:29] op_sel_hi:[1,0]
	v_pk_mul_f32 v[104:105], v[2:3], v[28:29] op_sel_hi:[1,0]
	v_pk_mul_f32 v[112:113], v[4:5], v[28:29] op_sel_hi:[1,0]
	ds_read_b128 v[2:5], v150 offset:60416
	ds_read_b128 v[34:37], v174 offset:32768
	ds_read_b128 v[38:41], v174 offset:32800
	ds_read_b128 v[42:45], v174 offset:32832
	ds_read_b128 v[46:49], v174 offset:32864
	v_cvt_pk_bf16_f32 v129, v168, v169
	v_cvt_pk_bf16_f32 v128, v82, v83
	v_cvt_pk_bf16_f32 v127, v160, v161
	v_cvt_pk_bf16_f32 v126, v158, v159
	v_cvt_pk_bf16_f32 v137, v24, v25
	v_cvt_pk_bf16_f32 v136, v166, v167
	v_cvt_pk_bf16_f32 v135, v164, v165
	s_waitcnt lgkmcnt(0)
	v_mfma_f32_32x32x16_bf16 v[86:101], v[2:5], v[126:129], v[34:49]
	v_cvt_pk_bf16_f32 v134, v162, v163
	v_mul_f32_e32 v84, v62, v68
	v_mul_f32_e32 v85, v63, v68
	v_mul_f32_e32 v170, v64, v68
	v_mul_f32_e32 v171, v65, v68
	v_pk_mul_f32 v[62:63], v[30:31], v[68:69] op_sel_hi:[1,0]
	v_pk_mul_f32 v[64:65], v[32:33], v[68:69] op_sel_hi:[1,0]
	v_pk_mul_f32 v[116:117], v[6:7], v[28:29] op_sel_hi:[1,0]
	v_pk_mul_f32 v[154:155], v[8:9], v[28:29] op_sel_hi:[1,0]
	v_mfma_f32_32x32x16_bf16 v[34:49], v[2:5], v[134:137], v[34:49]
	ds_read_b128 v[6:9], v150 offset:61440
	ds_read_b128 v[66:69], v174 offset:32896
	ds_read_b128 v[106:109], v150 offset:64512
	v_cvt_pk_bf16_f32 v125, v170, v171
	v_cvt_pk_bf16_f32 v124, v84, v85
	v_cvt_pk_bf16_f32 v123, v80, v81
	v_cvt_pk_bf16_f32 v122, v78, v79
	v_cvt_pk_bf16_f32 v149, v26, v27
	v_cvt_pk_bf16_f32 v148, v22, v23
	v_cvt_pk_bf16_f32 v147, v20, v21
	v_cvt_pk_bf16_f32 v146, v18, v19
	s_waitcnt lgkmcnt(2)
	v_mfma_f32_32x32x16_bf16 v[86:101], v[6:9], v[122:125], v[86:101]
	v_mul_f32_e32 v102, v10, v28
	v_mul_f32_e32 v103, v11, v28
	v_mul_f32_e32 v110, v12, v28
	v_mul_f32_e32 v111, v13, v28
	v_mul_f32_e32 v114, v14, v28
	v_mul_f32_e32 v115, v15, v28
	v_pk_mul_f32 v[156:157], v[16:17], v[28:29] op_sel_hi:[1,0]
	ds_read_b128 v[176:179], v174 offset:33536
	ds_read_b128 v[180:183], v174 offset:33568
	ds_read_b128 v[184:187], v174 offset:33600
	ds_read_b128 v[28:31], v174 offset:33632
	ds_read_b128 v[188:191], v174 offset:33792
	ds_read_b128 v[192:195], v174 offset:33824
	ds_read_b128 v[196:199], v174 offset:33856
	ds_read_b128 v[200:203], v174 offset:33888
	ds_read_b128 v[204:207], v150 offset:62464
	v_cvt_pk_bf16_f32 v133, v56, v57
	v_mfma_f32_32x32x16_bf16 v[34:49], v[6:9], v[146:149], v[34:49]
	v_cvt_pk_bf16_f32 v132, v54, v55
	v_cvt_pk_bf16_f32 v131, v52, v53
	v_cvt_pk_bf16_f32 v130, v50, v51
	ds_read_b128 v[70:73], v174 offset:33664
	ds_read_b128 v[74:77], v174 offset:33920
	ds_read_b128 v[208:211], v150 offset:63488
	v_cvt_pk_bf16_f32 v145, v154, v155
	v_cvt_pk_bf16_f32 v144, v116, v117
	v_cvt_pk_bf16_f32 v143, v112, v113
	v_cvt_pk_bf16_f32 v142, v104, v105
	s_waitcnt lgkmcnt(3)
	v_mfma_f32_32x32x16_bf16 v[86:101], v[204:207], v[130:133], v[86:101]
	v_cvt_pk_bf16_f32 v121, v64, v65
	v_cvt_pk_bf16_f32 v120, v62, v63
	v_cvt_pk_bf16_f32 v119, v60, v61
	v_cvt_pk_bf16_f32 v118, v58, v59
	v_cvt_pk_bf16_f32 v141, v156, v157
	v_cvt_pk_bf16_f32 v140, v114, v115
	v_cvt_pk_bf16_f32 v139, v110, v111
	v_mfma_f32_32x32x16_bf16 v[34:49], v[204:207], v[142:145], v[34:49]
	v_cvt_pk_bf16_f32 v138, v102, v103
	v_fma_f32 v16, v30, v170, v202
	v_fma_f32 v17, v31, v171, v203
	v_fma_f32 v14, v28, v84, v200
	v_fma_f32 v15, v29, v85, v201
	v_pk_fma_f32 v[12:13], v[186:187], v[80:81], v[198:199]
	v_pk_fma_f32 v[10:11], v[184:185], v[78:79], v[196:197]
	v_pk_fma_f32 v[8:9], v[182:183], v[168:169], v[194:195]
	s_waitcnt lgkmcnt(0)
	v_mfma_f32_32x32x16_bf16 v[86:101], v[208:211], v[118:121], v[86:101]
	v_fma_f32 v6, v180, v82, v192
	v_fma_f32 v7, v181, v83, v193
	ds_read_b128 v[78:81], v174 offset:33760
	ds_read_b128 v[82:85], v174 offset:33248
	v_fma_f32 v4, v178, v160, v190
	v_fma_f32 v5, v179, v161, v191
	v_pk_fma_f32 v[2:3], v[176:177], v[158:159], v[188:189]
	v_pk_fma_f32 v[32:33], v[30:31], v[26:27], v[202:203]
	v_pk_fma_f32 v[30:31], v[28:29], v[22:23], v[200:201]
	v_pk_fma_f32 v[28:29], v[186:187], v[20:21], v[198:199]
	v_pk_fma_f32 v[26:27], v[184:185], v[18:19], v[196:197]
	v_pk_fma_f32 v[24:25], v[182:183], v[24:25], v[194:195]
	v_pk_fma_f32 v[22:23], v[180:181], v[166:167], v[192:193]
	v_pk_fma_f32 v[20:21], v[178:179], v[164:165], v[190:191]
	v_pk_fma_f32 v[18:19], v[176:177], v[162:163], v[188:189]
	ds_read_b128 v[158:161], v174 offset:33696
	ds_read_b128 v[162:165], v174 offset:33728
	ds_read_b128 v[166:169], v174 offset:33952
	ds_read_b128 v[176:179], v174 offset:33984
	ds_read_b128 v[180:183], v174 offset:34016
	ds_read_b128 v[184:187], v212 offset:11264
	v_mfma_f32_32x32x16_bf16 v[34:49], v[208:211], v[138:141], v[34:49]
	v_cvt_pk_bf16_f32 v86, v86, v87
	v_cvt_pk_bf16_f32 v87, v88, v89
	v_cvt_pk_bf16_f32 v88, v90, v91
	v_cvt_pk_bf16_f32 v89, v92, v93
	ds_read_b128 v[90:93], v212 offset:12288
	v_pk_max_i16 v86, v86, 0
	v_pk_max_i16 v87, v87, 0
	v_pk_max_i16 v88, v88, 0
	v_pk_max_i16 v89, v89, 0
	s_nop 1
	s_nop 0
	v_cvt_pk_bf16_f32 v188, v34, v35
	v_cvt_pk_bf16_f32 v189, v36, v37
	v_cvt_pk_bf16_f32 v190, v38, v39
	v_cvt_pk_bf16_f32 v191, v40, v41
	s_waitcnt lgkmcnt(1)
	v_mfma_f32_32x32x16_bf16 v[2:17], v[184:187], v[86:89], v[2:17]
	v_pk_max_i16 v188, v188, 0
	v_pk_max_i16 v189, v189, 0
	v_pk_max_i16 v190, v190, 0
	v_pk_max_i16 v191, v191, 0
	v_cvt_pk_bf16_f32 v94, v94, v95
	v_cvt_pk_bf16_f32 v95, v96, v97
	v_cvt_pk_bf16_f32 v96, v98, v99
	v_cvt_pk_bf16_f32 v97, v100, v101
	v_cvt_pk_bf16_f32 v98, v42, v43
	v_cvt_pk_bf16_f32 v99, v44, v45
	v_mfma_f32_32x32x16_bf16 v[18:33], v[184:187], v[188:191], v[18:33]
	ds_read_b128 v[184:187], v212 offset:19456
	v_cvt_pk_bf16_f32 v100, v46, v47
	v_cvt_pk_bf16_f32 v101, v48, v49
	v_fma_f32 v64, v80, v64, v182
	v_fma_f32 v65, v81, v65, v183
	v_pk_fma_f32 v[62:63], v[78:79], v[62:63], v[180:181]
	v_pk_fma_f32 v[60:61], v[164:165], v[60:61], v[178:179]
	v_pk_fma_f32 v[58:59], v[162:163], v[58:59], v[176:177]
	v_pk_max_i16 v94, v94, 0
	v_pk_max_i16 v95, v95, 0
	v_pk_max_i16 v96, v96, 0
	v_pk_max_i16 v97, v97, 0
	v_pk_max_i16 v98, v98, 0
	v_pk_max_i16 v99, v99, 0
	v_pk_max_i16 v100, v100, 0
	v_pk_max_i16 v101, v101, 0
	v_pk_fma_f32 v[56:57], v[160:161], v[56:57], v[168:169]
	s_waitcnt lgkmcnt(1)
	v_mfma_f32_32x32x16_bf16 v[2:17], v[90:93], v[94:97], v[2:17]
	v_fma_f32 v54, v158, v54, v166
	v_fma_f32 v55, v159, v55, v167
	v_fma_f32 v52, v72, v52, v76
	v_fma_f32 v53, v73, v53, v77
	v_fma_f32 v50, v70, v50, v74
	v_fma_f32 v51, v71, v51, v75
	v_pk_fma_f32 v[48:49], v[80:81], v[156:157], v[182:183]
	v_pk_fma_f32 v[46:47], v[78:79], v[114:115], v[180:181]
	v_pk_fma_f32 v[44:45], v[164:165], v[110:111], v[178:179]
	v_pk_fma_f32 v[42:43], v[162:163], v[102:103], v[176:177]
	v_mfma_f32_32x32x16_bf16 v[18:33], v[90:93], v[98:101], v[18:33]
	ds_read_b128 v[90:93], v212 offset:20480
	v_fma_f32 v40, v160, v154, v168
	v_fma_f32 v41, v161, v155, v169
	v_fma_f32 v38, v158, v116, v166
	v_fma_f32 v39, v159, v117, v167
	v_pk_fma_f32 v[36:37], v[72:73], v[112:113], v[76:77]
	v_pk_fma_f32 v[34:35], v[70:71], v[104:105], v[74:75]
	s_waitcnt lgkmcnt(1)
	v_mfma_f32_32x32x16_bf16 v[50:65], v[184:187], v[86:89], v[50:65]
	ds_read_b128 v[70:73], v174 offset:32928
	ds_read_b128 v[74:77], v174 offset:32960
	ds_read_b128 v[78:81], v174 offset:32992
	ds_read_b128 v[86:89], v174 offset:33024
	ds_read_b128 v[110:113], v212 offset:1024
	v_mfma_f32_32x32x16_bf16 v[34:49], v[184:187], v[188:191], v[34:49]
	s_waitcnt lgkmcnt(5)
	v_mfma_f32_32x32x16_bf16 v[50:65], v[90:93], v[94:97], v[50:65]
	v_mfma_f32_32x32x16_bf16 v[34:49], v[90:93], v[98:101], v[34:49]
	s_waitcnt lgkmcnt(2)
	v_mfma_f32_32x32x16_bf16 v[90:105], v[106:109], v[126:129], v[66:81]
	v_mfma_f32_32x32x16_bf16 v[66:81], v[106:109], v[134:137], v[66:81]
	ds_read_b128 v[106:109], v212 offset:0
	s_waitcnt lgkmcnt(0)
	v_mfma_f32_32x32x16_bf16 v[90:105], v[106:109], v[122:125], v[90:105]
	v_mfma_f32_32x32x16_bf16 v[66:81], v[106:109], v[146:149], v[66:81]
	ds_read_b128 v[106:109], v212 offset:2048
	v_mfma_f32_32x32x16_bf16 v[90:105], v[110:113], v[130:133], v[90:105]
	v_mfma_f32_32x32x16_bf16 v[66:81], v[110:113], v[142:145], v[66:81]
	ds_read_b128 v[110:113], v212 offset:13312
	s_waitcnt lgkmcnt(1)
	v_mfma_f32_32x32x16_bf16 v[90:105], v[106:109], v[118:121], v[90:105]
	v_mfma_f32_32x32x16_bf16 v[66:81], v[106:109], v[138:141], v[66:81]
	s_nop 10
	v_cvt_pk_bf16_f32 v90, v90, v91
	v_cvt_pk_bf16_f32 v91, v92, v93
	v_cvt_pk_bf16_f32 v92, v94, v95
	v_cvt_pk_bf16_f32 v94, v98, v99
	v_cvt_pk_bf16_f32 v95, v100, v101
	ds_read_b128 v[98:101], v212 offset:21504
	v_cvt_pk_bf16_f32 v66, v66, v67
	v_cvt_pk_bf16_f32 v67, v68, v69
	v_cvt_pk_bf16_f32 v68, v70, v71
	v_cvt_pk_bf16_f32 v93, v96, v97
	v_cvt_pk_bf16_f32 v69, v72, v73
	ds_read_b128 v[70:73], v212 offset:14336
	v_pk_max_i16 v90, v90, 0
	v_pk_max_i16 v91, v91, 0
	v_pk_max_i16 v92, v92, 0
	v_pk_max_i16 v93, v93, 0
	v_pk_max_i16 v66, v66, 0
	v_pk_max_i16 v67, v67, 0
	v_pk_max_i16 v68, v68, 0
	v_pk_max_i16 v69, v69, 0
	v_cvt_pk_bf16_f32 v96, v102, v103
	s_waitcnt lgkmcnt(2)
	v_mfma_f32_32x32x16_bf16 v[2:17], v[110:113], v[90:93], v[2:17]
	v_cvt_pk_bf16_f32 v97, v104, v105
	v_cvt_pk_bf16_f32 v74, v74, v75
	v_cvt_pk_bf16_f32 v75, v76, v77
	v_cvt_pk_bf16_f32 v76, v78, v79
	v_cvt_pk_bf16_f32 v77, v80, v81
	v_pk_max_i16 v94, v94, 0
	v_pk_max_i16 v95, v95, 0
	v_pk_max_i16 v96, v96, 0
	v_pk_max_i16 v97, v97, 0
	v_pk_max_i16 v74, v74, 0
	v_pk_max_i16 v75, v75, 0
	v_pk_max_i16 v76, v76, 0
	v_pk_max_i16 v77, v77, 0
	v_mfma_f32_32x32x16_bf16 v[18:33], v[110:113], v[66:69], v[18:33]
	s_waitcnt lgkmcnt(1)
	v_mfma_f32_32x32x16_bf16 v[34:49], v[98:101], v[66:69], v[34:49]
	ds_read_b128 v[66:69], v212 offset:22528
	v_mfma_f32_32x32x16_bf16 v[50:65], v[98:101], v[90:93], v[50:65]
	s_waitcnt lgkmcnt(1)
	v_mfma_f32_32x32x16_bf16 v[2:17], v[70:73], v[94:97], v[2:17]
	v_mfma_f32_32x32x16_bf16 v[18:33], v[70:73], v[74:77], v[18:33]
	ds_read_b128 v[78:81], v212 offset:3072
	s_waitcnt lgkmcnt(1)
	v_mfma_f32_32x32x16_bf16 v[50:65], v[66:69], v[94:97], v[50:65]
	ds_read_b128 v[90:93], v174 offset:33056
	ds_read_b128 v[94:97], v174 offset:33088
	ds_read_b128 v[98:101], v174 offset:33120
	ds_read_b128 v[70:73], v174 offset:33152
	v_mfma_f32_32x32x16_bf16 v[34:49], v[66:69], v[74:77], v[34:49]
	ds_read_b128 v[66:69], v212 offset:4096
	ds_read_b128 v[74:77], v212 offset:5120
	s_waitcnt lgkmcnt(3)
	v_mfma_f32_32x32x16_bf16 v[102:117], v[78:81], v[126:129], v[86:101]
	v_mfma_f32_32x32x16_bf16 v[86:101], v[78:81], v[134:137], v[86:101]
	s_waitcnt lgkmcnt(1)
	v_mfma_f32_32x32x16_bf16 v[86:101], v[66:69], v[146:149], v[86:101]
	v_mfma_f32_32x32x16_bf16 v[102:117], v[66:69], v[122:125], v[102:117]
	ds_read_b128 v[66:69], v212 offset:6144
	s_waitcnt lgkmcnt(1)
	v_mfma_f32_32x32x16_bf16 v[86:101], v[74:77], v[142:145], v[86:101]
	v_mfma_f32_32x32x16_bf16 v[102:117], v[74:77], v[130:133], v[102:117]
	ds_read_b128 v[74:77], v212 offset:15360
	s_waitcnt lgkmcnt(1)
	v_mfma_f32_32x32x16_bf16 v[86:101], v[66:69], v[138:141], v[86:101]
	v_mfma_f32_32x32x16_bf16 v[102:117], v[66:69], v[118:121], v[102:117]
	s_nop 10
	v_cvt_pk_bf16_f32 v78, v86, v87
	v_cvt_pk_bf16_f32 v80, v90, v91
	v_cvt_pk_bf16_f32 v79, v88, v89
	v_cvt_pk_bf16_f32 v81, v92, v93
	ds_read_b128 v[86:89], v212 offset:16384
	ds_read_b128 v[90:93], v212 offset:23552
	v_cvt_pk_bf16_f32 v66, v102, v103
	v_cvt_pk_bf16_f32 v67, v104, v105
	v_cvt_pk_bf16_f32 v68, v106, v107
	v_cvt_pk_bf16_f32 v69, v108, v109
	v_pk_max_i16 v66, v66, 0
	v_pk_max_i16 v67, v67, 0
	v_pk_max_i16 v68, v68, 0
	v_pk_max_i16 v69, v69, 0
	v_pk_max_i16 v78, v78, 0
	v_pk_max_i16 v79, v79, 0
	v_pk_max_i16 v80, v80, 0
	v_pk_max_i16 v81, v81, 0
	v_cvt_pk_bf16_f32 v94, v94, v95
	s_waitcnt lgkmcnt(2)
	v_mfma_f32_32x32x16_bf16 v[18:33], v[74:77], v[78:81], v[18:33]
	v_cvt_pk_bf16_f32 v95, v96, v97
	v_cvt_pk_bf16_f32 v96, v98, v99
	v_cvt_pk_bf16_f32 v97, v100, v101
	v_pk_max_i16 v94, v94, 0
	v_pk_max_i16 v95, v95, 0
	v_pk_max_i16 v96, v96, 0
	v_pk_max_i16 v97, v97, 0
	v_mfma_f32_32x32x16_bf16 v[2:17], v[74:77], v[66:69], v[2:17]
	v_cvt_pk_bf16_f32 v74, v110, v111
	v_cvt_pk_bf16_f32 v75, v112, v113
	v_cvt_pk_bf16_f32 v76, v114, v115
	v_cvt_pk_bf16_f32 v77, v116, v117
	v_pk_max_i16 v74, v74, 0
	v_pk_max_i16 v75, v75, 0
	v_pk_max_i16 v76, v76, 0
	v_pk_max_i16 v77, v77, 0
	s_waitcnt lgkmcnt(0)
	v_mfma_f32_32x32x16_bf16 v[50:65], v[90:93], v[66:69], v[50:65]
	ds_read_b128 v[66:69], v212 offset:24576
	v_mfma_f32_32x32x16_bf16 v[34:49], v[90:93], v[78:81], v[34:49]
	ds_read_b128 v[102:105], v212 offset:7168
	v_mfma_f32_32x32x16_bf16 v[2:17], v[86:89], v[74:77], v[2:17]
	s_waitcnt lgkmcnt(1)
	v_mfma_f32_32x32x16_bf16 v[50:65], v[66:69], v[74:77], v[50:65]
	ds_read_b128 v[74:77], v174 offset:33184
	ds_read_b128 v[78:81], v174 offset:33216
	v_mfma_f32_32x32x16_bf16 v[34:49], v[66:69], v[94:97], v[34:49]
	ds_read_b128 v[66:69], v212 offset:8192
	v_mfma_f32_32x32x16_bf16 v[18:33], v[86:89], v[94:97], v[18:33]
	s_waitcnt lgkmcnt(1)
	v_mfma_f32_32x32x16_bf16 v[86:101], v[102:105], v[126:129], v[70:85]
	v_mfma_f32_32x32x16_bf16 v[70:85], v[102:105], v[134:137], v[70:85]
	ds_read_b128 v[102:105], v212 offset:9216
	v_lshlrev_b32_e32 v135, 2, v1
	v_add_u32_e32 v134, v172, v174
	s_waitcnt lgkmcnt(1)
	v_mfma_f32_32x32x16_bf16 v[86:101], v[66:69], v[122:125], v[86:101]
	v_mfma_f32_32x32x16_bf16 v[70:85], v[66:69], v[146:149], v[70:85]
	ds_read_b128 v[66:69], v212 offset:10240
	s_waitcnt lgkmcnt(1)
	v_mfma_f32_32x32x16_bf16 v[86:101], v[102:105], v[130:133], v[86:101]
	v_mfma_f32_32x32x16_bf16 v[70:85], v[102:105], v[142:145], v[70:85]
	ds_read_b128 v[102:105], v212 offset:17408
	s_waitcnt lgkmcnt(1)
	v_mfma_f32_32x32x16_bf16 v[86:101], v[66:69], v[118:121], v[86:101]
	v_mfma_f32_32x32x16_bf16 v[70:85], v[66:69], v[138:141], v[70:85]
	s_nop 10
	v_cvt_pk_bf16_f32 v68, v90, v91
	v_cvt_pk_bf16_f32 v69, v92, v93
	ds_read_b128 v[90:93], v212 offset:25600
	v_cvt_pk_bf16_f32 v66, v86, v87
	v_cvt_pk_bf16_f32 v67, v88, v89
	v_pk_max_i16 v66, v66, 0
	v_pk_max_i16 v67, v67, 0
	v_pk_max_i16 v68, v68, 0
	v_pk_max_i16 v69, v69, 0
	v_cvt_pk_bf16_f32 v70, v70, v71
	v_cvt_pk_bf16_f32 v71, v72, v73
	s_waitcnt lgkmcnt(1)
	v_mfma_f32_32x32x16_bf16 v[2:17], v[102:105], v[66:69], v[2:17]
	v_cvt_pk_bf16_f32 v72, v74, v75
	v_cvt_pk_bf16_f32 v73, v76, v77
	ds_read_b128 v[74:77], v212 offset:18432
	v_cvt_pk_bf16_f32 v86, v94, v95
	v_cvt_pk_bf16_f32 v87, v96, v97
	v_cvt_pk_bf16_f32 v88, v98, v99
	s_waitcnt lgkmcnt(1)
	v_mfma_f32_32x32x16_bf16 v[50:65], v[90:93], v[66:69], v[50:65]
	ds_read_b128 v[66:69], v212 offset:26624
	v_cvt_pk_bf16_f32 v89, v100, v101
	v_pk_max_i16 v86, v86, 0
	v_pk_max_i16 v87, v87, 0
	v_pk_max_i16 v88, v88, 0
	v_pk_max_i16 v89, v89, 0
	v_pk_max_i16 v70, v70, 0
	v_pk_max_i16 v71, v71, 0
	v_pk_max_i16 v72, v72, 0
	v_pk_max_i16 v73, v73, 0
	v_cvt_pk_bf16_f32 v78, v78, v79
	v_cvt_pk_bf16_f32 v79, v80, v81
	s_waitcnt lgkmcnt(1)
	v_mfma_f32_32x32x16_bf16 v[2:17], v[74:77], v[86:89], v[2:17]
	v_cvt_pk_bf16_f32 v80, v82, v83
	v_cvt_pk_bf16_f32 v81, v84, v85
	v_pk_max_i16 v78, v78, 0
	v_pk_max_i16 v79, v79, 0
	v_pk_max_i16 v80, v80, 0
	v_pk_max_i16 v81, v81, 0
	s_waitcnt lgkmcnt(0)
	v_mfma_f32_32x32x16_bf16 v[50:65], v[66:69], v[86:89], v[50:65]
	v_mfma_f32_32x32x16_bf16 v[34:49], v[90:93], v[70:73], v[34:49]
	s_nop 10
	v_add_f32_e32 v130, v10, v58
	v_add_f32_e32 v131, v11, v59
	v_add_f32_e32 v132, v12, v60
	v_add_f32_e32 v133, v13, v61
	v_add_f32_e32 v138, v4, v52
	v_add_f32_e32 v139, v5, v53
	v_pk_add_f32 v[140:141], v[16:17], v[64:65]
	v_pk_add_f32 v[142:143], v[8:9], v[56:57]
	v_pk_add_f32 v[144:145], v[14:15], v[62:63]
	v_pk_add_f32 v[146:147], v[6:7], v[54:55]
	v_mfma_f32_32x32x16_bf16 v[18:33], v[102:105], v[70:73], v[18:33]
	ds_read2st64_b32 v[70:71], v135 offset0:133 offset1:134
	v_add_f32_e32 v148, v2, v50
	v_add_f32_e32 v149, v3, v51
	v_add_f32_e32 v144, v146, v144
	v_add_f32_e32 v145, v147, v145
	v_pk_add_f32 v[140:141], v[142:143], v[140:141]
	v_pk_add_f32 v[132:133], v[138:139], v[132:133]
	v_pk_add_f32 v[130:131], v[148:149], v[130:131]
	v_pk_add_f32 v[132:133], v[132:133], v[140:141]
	v_pk_add_f32 v[130:131], v[130:131], v[144:145]
	v_mfma_f32_32x32x16_bf16 v[34:49], v[66:69], v[78:81], v[34:49]
	s_waitcnt vmcnt(0) lgkmcnt(0)
	v_mul_f32_e32 v66, v175, v70
	v_add_f32_e32 v130, v131, v130
	v_add_f32_e32 v131, v132, v133
	ds_write_b32 v173, v66 offset:512
	v_mul_f32_e32 v66, v175, v71
	v_add_f32_e32 v130, v130, v131
	s_waitcnt lgkmcnt(0)
	ds_read_b128 v[102:105], v174 offset:34560
	ds_read_b128 v[98:101], v174 offset:34592
	ds_read_b128 v[110:113], v174 offset:34624
	ds_read_b128 v[106:109], v174 offset:34656
	ds_read_b128 v[114:117], v174 offset:34688
	ds_read_b128 v[122:125], v174 offset:34720
	ds_read_b128 v[118:121], v174 offset:34752
	ds_read_b128 v[126:129], v174 offset:34784
	v_mov_b32_dpp v66, v66 quad_perm:[1,0,3,2] row_mask:0xf bank_mask:0xf bound_ctrl:1
	v_mov_b32_e32 v131, v130
	v_fmac_f32_e32 v66, v175, v71
	s_nop 0
	v_permlane32_swap_b32_e32 v130, v131
	v_add_f32_dpp v66, v66, v66 quad_perm:[2,3,0,1] row_mask:0xf bank_mask:0xf bound_ctrl:1
	v_add_f32_e32 v130, v130, v131
	v_fmamk_f32 v65, v130, 0xbc800000, v65
	v_add_f32_dpp v66, v66, v66 row_half_mirror row_mask:0xf bank_mask:0xf bound_ctrl:1
	v_fmamk_f32 v64, v130, 0xbc800000, v64
	v_fmamk_f32 v63, v130, 0xbc800000, v63
	v_fmamk_f32 v62, v130, 0xbc800000, v62
	v_fmamk_f32 v61, v130, 0xbc800000, v61
	v_fmamk_f32 v60, v130, 0xbc800000, v60
	v_fmamk_f32 v59, v130, 0xbc800000, v59
	v_fmamk_f32 v58, v130, 0xbc800000, v58
	v_fmamk_f32 v57, v130, 0xbc800000, v57
	v_fmamk_f32 v56, v130, 0xbc800000, v56
	v_fmamk_f32 v55, v130, 0xbc800000, v55
	v_fmamk_f32 v54, v130, 0xbc800000, v54
	v_fmamk_f32 v53, v130, 0xbc800000, v53
	v_fmamk_f32 v52, v130, 0xbc800000, v52
	v_fmamk_f32 v51, v130, 0xbc800000, v51
	v_fmac_f32_e32 v50, 0xbc800000, v130
	v_add_f32_dpp v66, v66, v66 row_ror:8 row_mask:0xf bank_mask:0xf bound_ctrl:1
	v_fmamk_f32 v17, v130, 0xbc800000, v17
	v_fmamk_f32 v16, v130, 0xbc800000, v16
	v_fmamk_f32 v15, v130, 0xbc800000, v15
	v_fmamk_f32 v14, v130, 0xbc800000, v14
	v_fmamk_f32 v13, v130, 0xbc800000, v13
	v_fmamk_f32 v12, v130, 0xbc800000, v12
	v_fmamk_f32 v11, v130, 0xbc800000, v11
	v_fmamk_f32 v10, v130, 0xbc800000, v10
	v_fmamk_f32 v9, v130, 0xbc800000, v9
	v_fmamk_f32 v8, v130, 0xbc800000, v8
	v_fmamk_f32 v7, v130, 0xbc800000, v7
	v_fmamk_f32 v6, v130, 0xbc800000, v6
	v_fmamk_f32 v5, v130, 0xbc800000, v5
	v_fmamk_f32 v4, v130, 0xbc800000, v4
	v_fmamk_f32 v3, v130, 0xbc800000, v3
	v_fmac_f32_e32 v2, 0xbc800000, v130
	v_pk_mul_f32 v[130:131], v[54:55], v[54:55]
	v_pk_mul_f32 v[132:133], v[62:63], v[62:63]
	v_pk_mul_f32 v[138:139], v[50:51], v[50:51]
	v_pk_mul_f32 v[140:141], v[58:59], v[58:59]
	v_pk_mul_f32 v[142:143], v[56:57], v[56:57]
	v_pk_mul_f32 v[144:145], v[64:65], v[64:65]
	v_pk_mul_f32 v[146:147], v[52:53], v[52:53]
	v_pk_mul_f32 v[148:149], v[60:61], v[60:61]
	v_mov_b32_e32 v67, v66
	v_pk_fma_f32 v[148:149], v[12:13], v[12:13], v[148:149]
	v_pk_fma_f32 v[146:147], v[4:5], v[4:5], v[146:147]
	v_pk_fma_f32 v[144:145], v[16:17], v[16:17], v[144:145]
	v_pk_fma_f32 v[142:143], v[8:9], v[8:9], v[142:143]
	v_pk_fma_f32 v[140:141], v[10:11], v[10:11], v[140:141]
	v_pk_fma_f32 v[138:139], v[2:3], v[2:3], v[138:139]
	v_pk_fma_f32 v[132:133], v[14:15], v[14:15], v[132:133]
	v_pk_fma_f32 v[130:131], v[6:7], v[6:7], v[130:131]
	v_permlane16_swap_b32_e32 v66, v67
	v_pk_add_f32 v[130:131], v[130:131], v[132:133]
	v_pk_add_f32 v[132:133], v[138:139], v[140:141]
	v_pk_add_f32 v[138:139], v[142:143], v[144:145]
	v_pk_add_f32 v[140:141], v[146:147], v[148:149]
	v_mfma_f32_32x32x16_bf16 v[18:33], v[74:77], v[78:81], v[18:33]
	v_add_f32_e32 v136, v66, v67
	ds_read_b128 v[70:73], v134 offset:512
	ds_read_b128 v[66:69], v134 offset:544
	ds_read_b128 v[78:81], v134 offset:576
	ds_read_b128 v[74:77], v134 offset:608
	ds_read_b128 v[82:85], v134 offset:640
	ds_read_b128 v[90:93], v134 offset:672
	ds_read_b128 v[86:89], v134 offset:704
	ds_read_b128 v[94:97], v134 offset:736
	v_pk_add_f32 v[138:139], v[140:141], v[138:139]
	v_pk_add_f32 v[130:131], v[132:133], v[130:131]
	s_waitcnt lgkmcnt(8)
	v_pk_mul_f32 v[140:141], v[126:127], v[62:63]
	v_pk_mov_b32 v[132:133], v[130:131], v[138:139] op_sel:[1,0]
	v_mov_b32_e32 v131, v139
	v_pk_mul_f32 v[138:139], v[122:123], v[54:55]
	v_pk_mul_f32 v[142:143], v[114:115], v[50:51]
	v_pk_mul_f32 v[144:145], v[118:119], v[58:59]
	v_pk_mul_f32 v[146:147], v[124:125], v[56:57]
	v_pk_mul_f32 v[148:149], v[128:129], v[64:65]
	v_pk_mul_f32 v[154:155], v[116:117], v[52:53]
	v_pk_mul_f32 v[156:157], v[120:121], v[60:61]
	v_pk_fma_f32 v[154:155], v[104:105], v[4:5], v[154:155]
	v_pk_fma_f32 v[156:157], v[112:113], v[12:13], v[156:157]
	v_pk_fma_f32 v[148:149], v[108:109], v[16:17], v[148:149]
	v_pk_fma_f32 v[146:147], v[100:101], v[8:9], v[146:147]
	v_pk_fma_f32 v[144:145], v[110:111], v[10:11], v[144:145]
	v_pk_fma_f32 v[142:143], v[102:103], v[2:3], v[142:143]
	v_pk_fma_f32 v[140:141], v[106:107], v[14:15], v[140:141]
	v_pk_fma_f32 v[138:139], v[98:99], v[6:7], v[138:139]
	v_pk_add_f32 v[130:131], v[132:133], v[130:131]
	v_pk_add_f32 v[138:139], v[138:139], v[140:141]
	v_pk_add_f32 v[140:141], v[142:143], v[144:145]
	v_pk_add_f32 v[142:143], v[146:147], v[148:149]
	v_pk_add_f32 v[144:145], v[154:155], v[156:157]
	v_pk_add_f32 v[132:133], v[130:131], v[130:131] op_sel:[0,1] op_sel_hi:[1,0]
	v_pk_add_f32 v[142:143], v[144:145], v[142:143]
	v_pk_add_f32 v[138:139], v[140:141], v[138:139]
	v_add_f32_e32 v133, v142, v143
	v_add_f32_e32 v130, v138, v139
	s_waitcnt lgkmcnt(2)
	v_pk_mul_f32 v[138:139], v[90:91], v[54:55]
	s_waitcnt lgkmcnt(0)
	v_pk_mul_f32 v[140:141], v[94:95], v[62:63]
	v_pk_mul_f32 v[142:143], v[82:83], v[50:51]
	v_pk_mul_f32 v[144:145], v[86:87], v[58:59]
	v_pk_mul_f32 v[146:147], v[92:93], v[56:57]
	v_pk_mul_f32 v[148:149], v[96:97], v[64:65]
	v_pk_mul_f32 v[154:155], v[84:85], v[52:53]
	v_pk_mul_f32 v[156:157], v[88:89], v[60:61]
	v_add_f32_e32 v130, v130, v133
	v_pk_fma_f32 v[156:157], v[80:81], v[12:13], v[156:157]
	v_pk_fma_f32 v[154:155], v[72:73], v[4:5], v[154:155]
	v_pk_fma_f32 v[148:149], v[76:77], v[16:17], v[148:149]
	v_pk_fma_f32 v[146:147], v[68:69], v[8:9], v[146:147]
	v_pk_fma_f32 v[144:145], v[78:79], v[10:11], v[144:145]
	v_pk_fma_f32 v[142:143], v[70:71], v[2:3], v[142:143]
	v_pk_fma_f32 v[140:141], v[74:75], v[14:15], v[140:141]
	v_pk_fma_f32 v[138:139], v[66:67], v[6:7], v[138:139]
	v_mov_b32_e32 v133, v130
	v_pk_add_f32 v[138:139], v[138:139], v[140:141]
	v_pk_add_f32 v[140:141], v[142:143], v[144:145]
	v_pk_add_f32 v[142:143], v[146:147], v[148:149]
	v_pk_add_f32 v[144:145], v[154:155], v[156:157]
	v_permlane32_swap_b32_e32 v130, v133
	v_pk_add_f32 v[142:143], v[144:145], v[142:143]
	v_add_f32_e32 v160, v130, v133
	v_pk_add_f32 v[138:139], v[140:141], v[138:139]
	v_add_f32_e32 v133, v142, v143
	v_pk_add_f32 v[140:141], v[26:27], v[42:43]
	v_pk_add_f32 v[142:143], v[28:29], v[44:45]
	v_pk_add_f32 v[144:145], v[20:21], v[36:37]
	v_pk_add_f32 v[146:147], v[32:33], v[48:49]
	v_pk_add_f32 v[148:149], v[24:25], v[40:41]
	v_pk_add_f32 v[154:155], v[30:31], v[46:47]
	v_pk_add_f32 v[156:157], v[22:23], v[38:39]
	v_pk_add_f32 v[158:159], v[18:19], v[34:35]
	v_pk_add_f32 v[154:155], v[156:157], v[154:155]
	v_pk_add_f32 v[146:147], v[148:149], v[146:147]
	v_pk_add_f32 v[142:143], v[144:145], v[142:143]
	v_pk_add_f32 v[140:141], v[158:159], v[140:141]
	v_pk_add_f32 v[142:143], v[142:143], v[146:147]
	v_pk_add_f32 v[140:141], v[140:141], v[154:155]
	v_add_f32_e32 v130, v138, v139
	v_add_f32_e32 v140, v141, v140
	v_add_f32_e32 v141, v142, v143
	v_add_f32_e32 v133, v130, v133
	v_add_f32_e32 v140, v140, v141
	v_mov_b32_e32 v131, v132
	v_mov_b32_e32 v130, v140
	s_nop 1
	v_permlane32_swap_b32_e32 v140, v130
	v_add_f32_e32 v130, v140, v130
	v_fmamk_f32 v49, v130, 0xbc800000, v49
	v_fmamk_f32 v48, v130, 0xbc800000, v48
	v_fmamk_f32 v47, v130, 0xbc800000, v47
	v_fmamk_f32 v46, v130, 0xbc800000, v46
	v_fmamk_f32 v45, v130, 0xbc800000, v45
	v_fmamk_f32 v44, v130, 0xbc800000, v44
	v_fmamk_f32 v43, v130, 0xbc800000, v43
	v_fmamk_f32 v42, v130, 0xbc800000, v42
	v_fmamk_f32 v41, v130, 0xbc800000, v41
	v_fmamk_f32 v40, v130, 0xbc800000, v40
	v_fmamk_f32 v39, v130, 0xbc800000, v39
	v_fmamk_f32 v38, v130, 0xbc800000, v38
	v_fmamk_f32 v37, v130, 0xbc800000, v37
	v_fmamk_f32 v36, v130, 0xbc800000, v36
	v_fmamk_f32 v35, v130, 0xbc800000, v35
	v_fmac_f32_e32 v34, 0xbc800000, v130
	v_fmamk_f32 v33, v130, 0xbc800000, v33
	v_fmamk_f32 v32, v130, 0xbc800000, v32
	v_fmamk_f32 v31, v130, 0xbc800000, v31
	v_fmamk_f32 v30, v130, 0xbc800000, v30
	v_fmamk_f32 v29, v130, 0xbc800000, v29
	v_fmamk_f32 v28, v130, 0xbc800000, v28
	v_fmamk_f32 v27, v130, 0xbc800000, v27
	v_fmamk_f32 v26, v130, 0xbc800000, v26
	v_fmamk_f32 v25, v130, 0xbc800000, v25
	v_fmamk_f32 v24, v130, 0xbc800000, v24
	v_fmamk_f32 v23, v130, 0xbc800000, v23
	v_fmamk_f32 v22, v130, 0xbc800000, v22
	v_fmamk_f32 v21, v130, 0xbc800000, v21
	v_fmamk_f32 v20, v130, 0xbc800000, v20
	v_fmamk_f32 v19, v130, 0xbc800000, v19
	v_fmac_f32_e32 v18, 0xbc800000, v130
	v_pk_mul_f32 v[140:141], v[38:39], v[38:39]
	v_pk_mul_f32 v[142:143], v[46:47], v[46:47]
	v_pk_mul_f32 v[144:145], v[34:35], v[34:35]
	v_pk_mul_f32 v[146:147], v[42:43], v[42:43]
	v_pk_mul_f32 v[148:149], v[40:41], v[40:41]
	v_pk_mul_f32 v[154:155], v[48:49], v[48:49]
	v_pk_mul_f32 v[156:157], v[36:37], v[36:37]
	v_pk_mul_f32 v[158:159], v[44:45], v[44:45]
	v_pk_fma_f32 v[156:157], v[20:21], v[20:21], v[156:157]
	v_pk_fma_f32 v[158:159], v[28:29], v[28:29], v[158:159]
	v_pk_fma_f32 v[154:155], v[32:33], v[32:33], v[154:155]
	v_pk_fma_f32 v[148:149], v[24:25], v[24:25], v[148:149]
	v_pk_fma_f32 v[146:147], v[26:27], v[26:27], v[146:147]
	v_pk_fma_f32 v[144:145], v[18:19], v[18:19], v[144:145]
	v_pk_fma_f32 v[142:143], v[30:31], v[30:31], v[142:143]
	v_pk_fma_f32 v[140:141], v[22:23], v[22:23], v[140:141]
	v_permlane32_swap_b32_e32 v132, v131
	v_pk_add_f32 v[140:141], v[140:141], v[142:143]
	v_pk_add_f32 v[142:143], v[144:145], v[146:147]
	v_pk_add_f32 v[144:145], v[148:149], v[154:155]
	v_pk_add_f32 v[146:147], v[156:157], v[158:159]
	v_pk_add_f32 v[140:141], v[142:143], v[140:141]
	v_pk_add_f32 v[144:145], v[146:147], v[144:145]
	v_pk_mul_f32 v[122:123], v[122:123], v[38:39]
	v_pk_mov_b32 v[142:143], v[140:141], v[144:145] op_sel:[1,0]
	v_mov_b32_e32 v141, v145
	v_pk_add_f32 v[140:141], v[142:143], v[140:141]
	v_pk_mul_f32 v[126:127], v[126:127], v[46:47]
	v_pk_add_f32 v[140:141], v[140:141], v[140:141] op_sel:[0,1] op_sel_hi:[1,0]
	v_pk_mul_f32 v[114:115], v[114:115], v[34:35]
	v_mov_b32_e32 v130, v140
	s_nop 1
	v_permlane32_swap_b32_e32 v140, v130
	v_mov_b32_e32 v141, v132
	v_pk_add_f32 v[130:131], v[140:141], v[130:131]
	v_pk_mul_f32 v[118:119], v[118:119], v[42:43]
	v_pk_fma_f32 v[130:131], v[130:131], s[0:1], v[152:153] op_sel_hi:[1,0,0]
	v_pk_mul_f32 v[124:125], v[124:125], v[40:41]
	v_pk_mul_f32 v[128:129], v[128:129], v[48:49]
	v_pk_mul_f32 v[116:117], v[116:117], v[36:37]
	v_pk_mul_f32 v[120:121], v[120:121], v[44:45]
	v_pk_fma_f32 v[112:113], v[112:113], v[28:29], v[120:121]
	v_pk_fma_f32 v[104:105], v[104:105], v[20:21], v[116:117]
	v_pk_fma_f32 v[108:109], v[108:109], v[32:33], v[128:129]
	v_pk_fma_f32 v[100:101], v[100:101], v[24:25], v[124:125]
	v_pk_fma_f32 v[110:111], v[110:111], v[26:27], v[118:119]
	v_pk_fma_f32 v[102:103], v[102:103], v[18:19], v[114:115]
	v_pk_fma_f32 v[106:107], v[106:107], v[30:31], v[126:127]
	v_pk_fma_f32 v[98:99], v[98:99], v[22:23], v[122:123]
	v_rsq_f32_e32 v131, v131
	v_pk_add_f32 v[98:99], v[98:99], v[106:107]
	v_pk_add_f32 v[102:103], v[102:103], v[110:111]
	v_pk_add_f32 v[100:101], v[100:101], v[108:109]
	v_pk_add_f32 v[104:105], v[104:105], v[112:113]
	v_rsq_f32_e32 v132, v130
	v_pk_add_f32 v[100:101], v[104:105], v[100:101]
	v_pk_add_f32 v[98:99], v[102:103], v[98:99]
	v_add_f32_e32 v98, v98, v99
	v_add_f32_e32 v99, v100, v101
	v_add_f32_e32 v98, v98, v99
	v_mov_b32_e32 v99, v98
	v_pk_mul_f32 v[90:91], v[90:91], v[38:39]
	v_pk_mul_f32 v[94:95], v[94:95], v[46:47]
	v_pk_mul_f32 v[82:83], v[82:83], v[34:35]
	v_pk_mul_f32 v[86:87], v[86:87], v[42:43]
	v_permlane32_swap_b32_e32 v98, v99
	v_pk_fma_f32 v[78:79], v[78:79], v[26:27], v[86:87]
	v_pk_fma_f32 v[70:71], v[70:71], v[18:19], v[82:83]
	v_pk_fma_f32 v[74:75], v[74:75], v[30:31], v[94:95]
	v_pk_fma_f32 v[66:67], v[66:67], v[22:23], v[90:91]
	v_mov_b32_e32 v130, v131
	v_mov_b32_e32 v131, v132
	v_add_f32_e32 v98, v98, v99
	v_pk_add_f32 v[66:67], v[66:67], v[74:75]
	v_pk_add_f32 v[70:71], v[70:71], v[78:79]
	v_mul_f32_e32 v139, v160, v130
	v_mul_f32_e32 v98, v98, v131
	v_pk_add_f32 v[66:67], v[70:71], v[66:67]
	v_cmp_gt_u32_e32 vcc, 32, v1
	v_add_f32_e32 v66, v66, v67
	v_pk_mul_f32 v[92:93], v[92:93], v[40:41]
	v_cndmask_b32_e32 v67, v98, v139, vcc
	v_add_f32_e32 v67, s12, v67
	v_pk_mul_f32 v[96:97], v[96:97], v[48:49]
	v_pk_mul_f32 v[84:85], v[84:85], v[36:37]
	v_pk_mul_f32 v[88:89], v[88:89], v[44:45]
	v_mul_f32_e32 v67, 0xbfb8aa3b, v67
	v_pk_fma_f32 v[80:81], v[80:81], v[28:29], v[88:89]
	v_pk_fma_f32 v[72:73], v[72:73], v[20:21], v[84:85]
	v_pk_fma_f32 v[76:77], v[76:77], v[32:33], v[96:97]
	v_pk_fma_f32 v[68:69], v[68:69], v[24:25], v[92:93]
	v_exp_f32_e32 v70, v67
	v_pk_add_f32 v[68:69], v[68:69], v[76:77]
	v_pk_add_f32 v[72:73], v[72:73], v[80:81]
	v_cmp_lt_i32_e64 s[0:1], 0, v151
	v_pk_add_f32 v[68:69], v[72:73], v[68:69]
	v_mov_b32_e32 v137, v136
	v_add_f32_e32 v67, v68, v69
	v_add_f32_e32 v67, v66, v67
	v_add_f32_e32 v66, 1.0, v70
	v_rcp_f32_e32 v66, v66
	v_mov_b32_e32 v69, 0xff800000
	v_mov_b32_e32 v138, v133
	v_mov_b32_e32 v68, v67
	v_cndmask_b32_e64 v70, v69, v66, s[0:1]
	v_mbcnt_lo_u32_b32 v66, -1, 0
	v_mbcnt_hi_u32_b32 v66, -1, v66
	v_permlane32_swap_b32_e32 v136, v137
	v_permlane32_swap_b32_e32 v133, v138
	v_permlane32_swap_b32_e32 v67, v68
	v_and_b32_e32 v86, 64, v66
	s_mov_b32 s14, 8
	s_mov_b32 s13, 0
	v_mov_b32_e32 v66, 0
	s_waitcnt lgkmcnt(0)
